# prio_remain
# speedup vs baseline: 1.0392x; 1.0392x over previous
.LBB0_30:
	s_or_b64 exec, exec, s[22:23]
	v_mul_lo_u16_e32 v49, 3, v49
	v_sub_u16_e32 v48, v48, v49
	v_mov_b32_e32 v49, 1
	s_waitcnt vmcnt(5)
	v_pk_mul_f32 v[22:23], v[22:23], v[44:45] op_sel_hi:[1,0]
	v_pk_mul_f32 v[24:25], v[24:25], v[44:45] op_sel_hi:[1,0]
	s_waitcnt vmcnt(4)
	v_pk_mul_f32 v[18:19], v[18:19], v[44:45] op_sel_hi:[1,0]
	v_mov_b32_e32 v51, 0xbf2562dd
	v_mov_b32_e32 v52, 0xbfa562dd
	v_cmp_eq_u16_sdwa s[0:1], v48, v49 src0_sel:BYTE_0 src1_sel:DWORD
	v_cvt_pk_f16_f32 v22, v22, v23
	v_cvt_pk_f16_f32 v23, v24, v25
	v_cvt_pk_f16_f32 v24, v18, v19
	v_pk_mul_f32 v[18:19], v[20:21], v[44:45] op_sel_hi:[1,0]
	v_cndmask_b32_e64 v48, v51, v52, s[0:1]
	v_cvt_pk_f16_f32 v25, v18, v19
	v_lshlrev_b32_e32 v18, 4, v0
	ds_write_b128 v18, v[22:25]
	s_waitcnt vmcnt(3)
	v_pk_mul_f32 v[20:21], v[48:49], v[30:31] op_sel_hi:[0,1]
	v_pk_mul_f32 v[22:23], v[48:49], v[32:33] op_sel_hi:[0,1]
	v_cvt_pk_f16_f32 v20, v20, v21
	v_cvt_pk_f16_f32 v21, v22, v23
	s_waitcnt vmcnt(2)
	v_pk_mul_f32 v[22:23], v[48:49], v[26:27] op_sel_hi:[0,1]
	v_pk_mul_f32 v[24:25], v[48:49], v[28:29] op_sel_hi:[0,1]
	v_cvt_pk_f16_f32 v22, v22, v23
	v_cvt_pk_f16_f32 v23, v24, v25
	v_lshlrev_b32_e32 v19, 4, v45
	ds_write_b128 v19, v[20:23]
	s_waitcnt vmcnt(1)
	v_pk_mul_f32 v[20:21], v[38:39], v[46:47] op_sel_hi:[1,0]
	v_pk_mul_f32 v[22:23], v[40:41], v[46:47] op_sel_hi:[1,0]
	v_cvt_pk_f16_f32 v20, v20, v21
	v_cvt_pk_f16_f32 v21, v22, v23
	s_waitcnt vmcnt(0)
	v_pk_mul_f32 v[22:23], v[34:35], v[46:47] op_sel_hi:[1,0]
	v_pk_mul_f32 v[24:25], v[36:37], v[46:47] op_sel_hi:[1,0]
	v_and_b32_e32 v69, 63, v0
	v_cvt_pk_f16_f32 v22, v22, v23
	v_cvt_pk_f16_f32 v23, v24, v25
	v_lshlrev_b32_e32 v19, 4, v47
	ds_write_b128 v19, v[20:23]
	s_and_saveexec_b64 s[0:1], vcc
	v_mad_i32_i24 v18, v0, -12, v18
	ds_write_b32 v18, v50 offset:41984
	s_or_b64 exec, exec, s[0:1]
	s_waitcnt lgkmcnt(0)
	s_load_dword s0, s[12:13], 0x0
	v_mov_b32_e32 v18, 0xbfb8aa3b
	s_lshl_b32 s3, s21, 4
	s_cmpk_gt_i32 s20, 0x7fff
	v_cmp_gt_u32_e32 vcc, 32, v69
	s_waitcnt lgkmcnt(0)
	v_mul_f32_e32 v18, s0, v18
	v_exp_f32_e32 v70, v18
	v_mov_b32_e32 v18, 0
	v_and_b32_e32 v71, 48, v0
	s_mov_b32 s10, s20
	s_barrier
	s_cbranch_scc1 .LBB0_37
	s_sub_i32 s2, s20, s3
	s_add_i32 s9, s3, s20
	s_mov_b32 s4, 1.0
	s_mov_b32 s8, 0x3fb4c4be
	v_lshlrev_b32_e32 v72, 4, v69
	v_cmp_eq_u32_e64 s[0:1], 1, v1
	v_lshl_add_u32 v38, s2, 5, v69
	s_lshl_b32 s7, s21, 9
	v_mov_b32_e32 v18, 0
	s_mov_b32 s12, 0
	s_mov_b32 s2, 0x4a000000
	s_mov_b32 s5, s4
	s_mov_b32 s6, 0x3f34c4be
	v_mov_b64_e32 v[40:41], s[8:9]
	s_mov_b32 s8, 0x400a34e2
	s_mov_b32 s33, 0
	s_branch .LBB0_35

.LBB0_35:
	s_setprio 3
	s_cmp_lt_u32 s33, 5
	s_cbranch_scc1 .Lprio_done
	s_setprio 2
	s_cmp_lt_u32 s33, 6
	s_cbranch_scc1 .Lprio_done
	s_setprio 1
	s_cmp_lt_u32 s33, 7
	s_cbranch_scc1 .Lprio_done
	s_setprio 0
.Lprio_done:
	s_add_u32 s33, s33, 1
	s_cmp_lg_u32 s12, 0
	s_cselect_b64 s[10:11], -1, 0
	s_and_b64 s[16:17], s[10:11], vcc
	s_and_saveexec_b64 s[10:11], s[16:17]
	s_cbranch_execz .LBB0_34
	v_exp_f32_e32 v0, v18
	v_ashrrev_i32_e32 v39, 31, v38
	v_fma_f32 v0, v0, v70, 1.0
	v_rcp_f32_e32 v18, v0
	v_lshl_add_u64 v[0:1], v[38:39], 2, s[14:15]
	global_store_dword v[0:1], v18, off
	s_branch .LBB0_34

	.amdhsa_kernel _Z10lstm_fusedPKfS0_S0_S0_S0_S0_S0_S0_S0_S0_S0_Pf
		.amdhsa_group_segment_fixed_size 43648
		.amdhsa_private_segment_fixed_size 0
		.amdhsa_kernarg_size 352
		.amdhsa_user_sgpr_count 2
		.amdhsa_user_sgpr_dispatch_ptr 0
		.amdhsa_user_sgpr_queue_ptr 0
		.amdhsa_user_sgpr_kernarg_segment_ptr 1
		.amdhsa_user_sgpr_dispatch_id 0
		.amdhsa_user_sgpr_kernarg_preload_length 0
		.amdhsa_user_sgpr_kernarg_preload_offset 0
		.amdhsa_user_sgpr_private_segment_size 0
		.amdhsa_uses_dynamic_stack 0
		.amdhsa_enable_private_segment 0
		.amdhsa_system_sgpr_workgroup_id_x 1
		.amdhsa_system_sgpr_workgroup_id_y 0
		.amdhsa_system_sgpr_workgroup_id_z 0
		.amdhsa_system_sgpr_workgroup_info 0
		.amdhsa_system_vgpr_workitem_id 0
		.amdhsa_next_free_vgpr 128
		.amdhsa_next_free_sgpr 34
		.amdhsa_accum_offset 128
		.amdhsa_reserve_vcc 1
		.amdhsa_float_round_mode_32 0
		.amdhsa_float_round_mode_16_64 0
		.amdhsa_float_denorm_mode_32 3
		.amdhsa_float_denorm_mode_16_64 3
		.amdhsa_dx10_clamp 1
		.amdhsa_ieee_mode 1
		.amdhsa_fp16_overflow 0
		.amdhsa_tg_split 0
		.amdhsa_exception_fp_ieee_invalid_op 0
		.amdhsa_exception_fp_denorm_src 0
		.amdhsa_exception_fp_ieee_div_zero 0
		.amdhsa_exception_fp_ieee_overflow 0
		.amdhsa_exception_fp_ieee_underflow 0
		.amdhsa_exception_fp_ieee_inexact 0
		.amdhsa_exception_int_div_zero 0
	.end_amdhsa_kernel

amdhsa.kernels:
  - .agpr_count:     0
    .args:
      - .actual_access:  read_only
        .address_space:  global
        .offset:         0
        .size:           8
        .value_kind:     global_buffer
      - .actual_access:  read_only
        .address_space:  global
        .offset:         8
        .size:           8
        .value_kind:     global_buffer
      - .actual_access:  read_only
        .address_space:  global
        .offset:         16
        .size:           8
        .value_kind:     global_buffer
      - .actual_access:  read_only
        .address_space:  global
        .offset:         24
        .size:           8
        .value_kind:     global_buffer
      - .actual_access:  read_only
        .address_space:  global
        .offset:         32
        .size:           8
        .value_kind:     global_buffer
      - .actual_access:  read_only
        .address_space:  global
        .offset:         40
        .size:           8
        .value_kind:     global_buffer
      - .actual_access:  read_only
        .address_space:  global
        .offset:         48
        .size:           8
        .value_kind:     global_buffer
      - .actual_access:  read_only
        .address_space:  global
        .offset:         56
        .size:           8
        .value_kind:     global_buffer
      - .actual_access:  read_only
        .address_space:  global
        .offset:         64
        .size:           8
        .value_kind:     global_buffer
      - .actual_access:  read_only
        .address_space:  global
        .offset:         72
        .size:           8
        .value_kind:     global_buffer
      - .actual_access:  read_only
        .address_space:  global
        .offset:         80
        .size:           8
        .value_kind:     global_buffer
      - .actual_access:  write_only
        .address_space:  global
        .offset:         88
        .size:           8
        .value_kind:     global_buffer
      - .offset:         96
        .size:           4
        .value_kind:     hidden_block_count_x
      - .offset:         100
        .size:           4
        .value_kind:     hidden_block_count_y
      - .offset:         104
        .size:           4
        .value_kind:     hidden_block_count_z
      - .offset:         108
        .size:           2
        .value_kind:     hidden_group_size_x
      - .offset:         110
        .size:           2
        .value_kind:     hidden_group_size_y
      - .offset:         112
        .size:           2
        .value_kind:     hidden_group_size_z
      - .offset:         114
        .size:           2
        .value_kind:     hidden_remainder_x
      - .offset:         116
        .size:           2
        .value_kind:     hidden_remainder_y
      - .offset:         118
        .size:           2
        .value_kind:     hidden_remainder_z
      - .offset:         136
        .size:           8
        .value_kind:     hidden_global_offset_x
      - .offset:         144
        .size:           8
        .value_kind:     hidden_global_offset_y
      - .offset:         152
        .size:           8
        .value_kind:     hidden_global_offset_z
      - .offset:         160
        .size:           2
        .value_kind:     hidden_grid_dims
    .group_segment_fixed_size: 43648
    .kernarg_segment_align: 8
    .kernarg_segment_size: 352
    .language:       OpenCL C
    .language_version:
      - 2
      - 0
    .max_flat_workgroup_size: 1024
    .name:           _Z10lstm_fusedPKfS0_S0_S0_S0_S0_S0_S0_S0_S0_S0_Pf
    .private_segment_fixed_size: 0
    .sgpr_count:     40
    .sgpr_spill_count: 0
    .symbol:         _Z10lstm_fusedPKfS0_S0_S0_S0_S0_S0_S0_S0_S0_S0_Pf.kd
    .uniform_work_group_size: 1
    .uses_dynamic_stack: false
    .vgpr_count:     128
    .vgpr_spill_count: 0
    .wavefront_size: 64
